# gcn layer-2 fast path: recompute-MFMA results alternate between two register tuples so the next tile's MFMAs issue before the current tile's epilogue (removes the wait states)
# speedup vs baseline: 1.0761x; 1.0064x over previous
.LBB5_22:
	s_or_b64 exec, exec, s[14:15]
	v_lshl_or_b32 v74, v74, 6, v109
	global_load_dwordx4 v[74:77], v74, s[10:11]
	s_waitcnt vmcnt(1)
	v_mfma_f32_16x16x32_f16 v[112:115], v[70:73], v[32:35], 0
	v_mfma_f32_16x16x32_f16 v[120:123], v[70:73], v[36:39], 0
	v_add_u32_e32 v93, -1, v93
	s_add_i32 s29, s29, 32
	s_add_i32 s28, s28, 2
	v_cmp_eq_u32_e32 vcc, 0, v93
	v_add_u32_e32 v106, 0x100, v106
	s_waitcnt vmcnt(0)
	v_mfma_f32_16x16x32_f16 v[116:119], v[74:77], v[32:35], 0
	s_nop 1
	s_or_b64 s[12:13], vcc, s[12:13]
	s_nop 5
	v_add_f32_e32 v116, v65, v116
	v_add_f32_e32 v117, v65, v117
	v_add_f32_e32 v118, v65, v118
	v_add_f32_e32 v119, v65, v119
	v_add_f32_e32 v112, v65, v112
	v_add_f32_e32 v113, v65, v113
	v_add_f32_e32 v114, v65, v114
	v_add_f32_e32 v115, v65, v115
	v_cvt_pk_f16_f32 v112, v112, v113
	v_cvt_pk_f16_f32 v113, v114, v115
	v_cvt_pk_f16_f32 v114, v116, v117
	v_cvt_pk_f16_f32 v115, v118, v119
	v_mfma_f32_16x16x32_f16 v[116:119], v[74:77], v[36:39], 0
	v_pk_max_f16 v112, v112, 0
	v_pk_max_f16 v113, v113, 0
	v_pk_max_f16 v114, v114, 0
	v_pk_max_f16 v115, v115, 0
	s_nop 1
	v_mfma_f32_16x16x32_f16 v[28:31], v[112:115], v[66:69], v[28:31]
	v_mfma_f32_16x16x32_f16 v[112:115], v[70:73], v[40:43], 0
	v_add_f32_e32 v116, v94, v116
	v_add_f32_e32 v117, v94, v117
	v_add_f32_e32 v118, v94, v118
	v_add_f32_e32 v119, v94, v119
	v_add_f32_e32 v120, v94, v120
	v_add_f32_e32 v121, v94, v121
	v_add_f32_e32 v122, v94, v122
	v_add_f32_e32 v123, v94, v123
	v_cvt_pk_f16_f32 v120, v120, v121
	v_cvt_pk_f16_f32 v121, v122, v123
	v_cvt_pk_f16_f32 v122, v116, v117
	v_cvt_pk_f16_f32 v123, v118, v119
	v_mfma_f32_16x16x32_f16 v[116:119], v[74:77], v[40:43], 0
	v_pk_max_f16 v120, v120, 0
	v_pk_max_f16 v121, v121, 0
	v_pk_max_f16 v122, v122, 0
	v_pk_max_f16 v123, v123, 0
	s_nop 1
	v_mfma_f32_16x16x32_f16 v[24:27], v[120:123], v[66:69], v[24:27]
	v_mfma_f32_16x16x32_f16 v[120:123], v[70:73], v[44:47], 0
	v_add_f32_e32 v116, v95, v116
	v_add_f32_e32 v117, v95, v117
	v_add_f32_e32 v118, v95, v118
	v_add_f32_e32 v119, v95, v119
	v_add_f32_e32 v112, v95, v112
	v_add_f32_e32 v113, v95, v113
	v_add_f32_e32 v114, v95, v114
	v_add_f32_e32 v115, v95, v115
	v_cvt_pk_f16_f32 v112, v112, v113
	v_cvt_pk_f16_f32 v113, v114, v115
	v_cvt_pk_f16_f32 v114, v116, v117
	v_cvt_pk_f16_f32 v115, v118, v119
	v_mfma_f32_16x16x32_f16 v[116:119], v[74:77], v[44:47], 0
	v_pk_max_f16 v112, v112, 0
	v_pk_max_f16 v113, v113, 0
	v_pk_max_f16 v114, v114, 0
	v_pk_max_f16 v115, v115, 0
	s_nop 1
	v_mfma_f32_16x16x32_f16 v[20:23], v[112:115], v[66:69], v[20:23]
	v_mfma_f32_16x16x32_f16 v[112:115], v[70:73], v[48:51], 0
	v_add_f32_e32 v116, v96, v116
	v_add_f32_e32 v117, v96, v117
	v_add_f32_e32 v118, v96, v118
	v_add_f32_e32 v119, v96, v119
	v_add_f32_e32 v120, v96, v120
	v_add_f32_e32 v121, v96, v121
	v_add_f32_e32 v122, v96, v122
	v_add_f32_e32 v123, v96, v123
	v_cvt_pk_f16_f32 v120, v120, v121
	v_cvt_pk_f16_f32 v121, v122, v123
	v_cvt_pk_f16_f32 v122, v116, v117
	v_cvt_pk_f16_f32 v123, v118, v119
	v_mfma_f32_16x16x32_f16 v[116:119], v[74:77], v[48:51], 0
	v_pk_max_f16 v120, v120, 0
	v_pk_max_f16 v121, v121, 0
	v_pk_max_f16 v122, v122, 0
	v_pk_max_f16 v123, v123, 0
	s_nop 1
	v_mfma_f32_16x16x32_f16 v[16:19], v[120:123], v[66:69], v[16:19]
	v_mfma_f32_16x16x32_f16 v[120:123], v[70:73], v[52:55], 0
	v_add_f32_e32 v116, v97, v116
	v_add_f32_e32 v117, v97, v117
	v_add_f32_e32 v118, v97, v118
	v_add_f32_e32 v119, v97, v119
	v_add_f32_e32 v112, v97, v112
	v_add_f32_e32 v113, v97, v113
	v_add_f32_e32 v114, v97, v114
	v_add_f32_e32 v115, v97, v115
	v_cvt_pk_f16_f32 v112, v112, v113
	v_cvt_pk_f16_f32 v113, v114, v115
	v_cvt_pk_f16_f32 v114, v116, v117
	v_cvt_pk_f16_f32 v115, v118, v119
	v_mfma_f32_16x16x32_f16 v[116:119], v[74:77], v[52:55], 0
	v_pk_max_f16 v112, v112, 0
	v_pk_max_f16 v113, v113, 0
	v_pk_max_f16 v114, v114, 0
	v_pk_max_f16 v115, v115, 0
	s_nop 1
	v_mfma_f32_16x16x32_f16 v[12:15], v[112:115], v[66:69], v[12:15]
	v_mfma_f32_16x16x32_f16 v[112:115], v[70:73], v[56:59], 0
	v_add_f32_e32 v116, v98, v116
	v_add_f32_e32 v117, v98, v117
	v_add_f32_e32 v118, v98, v118
	v_add_f32_e32 v119, v98, v119
	v_add_f32_e32 v120, v98, v120
	v_add_f32_e32 v121, v98, v121
	v_add_f32_e32 v122, v98, v122
	v_add_f32_e32 v123, v98, v123
	v_cvt_pk_f16_f32 v120, v120, v121
	v_cvt_pk_f16_f32 v121, v122, v123
	v_cvt_pk_f16_f32 v122, v116, v117
	v_cvt_pk_f16_f32 v123, v118, v119
	v_mfma_f32_16x16x32_f16 v[116:119], v[74:77], v[56:59], 0
	v_pk_max_f16 v120, v120, 0
	v_pk_max_f16 v121, v121, 0
	v_pk_max_f16 v122, v122, 0
	v_pk_max_f16 v123, v123, 0
	s_nop 1
	v_mfma_f32_16x16x32_f16 v[8:11], v[120:123], v[66:69], v[8:11]
	v_mfma_f32_16x16x32_f16 v[120:123], v[70:73], v[60:63], 0
	v_add_f32_e32 v116, v99, v116
	v_add_f32_e32 v117, v99, v117
	v_add_f32_e32 v118, v99, v118
	v_add_f32_e32 v119, v99, v119
	v_add_f32_e32 v112, v99, v112
	v_add_f32_e32 v113, v99, v113
	v_add_f32_e32 v114, v99, v114
	v_add_f32_e32 v115, v99, v115
	v_cvt_pk_f16_f32 v112, v112, v113
	v_cvt_pk_f16_f32 v113, v114, v115
	v_cvt_pk_f16_f32 v114, v116, v117
	v_cvt_pk_f16_f32 v115, v118, v119
	v_mfma_f32_16x16x32_f16 v[116:119], v[74:77], v[60:63], 0
	v_pk_max_f16 v112, v112, 0
	v_pk_max_f16 v113, v113, 0
	v_pk_max_f16 v114, v114, 0
	v_pk_max_f16 v115, v115, 0
	s_nop 1
	v_mfma_f32_16x16x32_f16 v[4:7], v[112:115], v[66:69], v[4:7]
	s_nop 0
	v_add_f32_e32 v116, v100, v116
	v_add_f32_e32 v117, v100, v117
	v_add_f32_e32 v118, v100, v118
	v_add_f32_e32 v119, v100, v119
	v_add_f32_e32 v120, v100, v120
	v_add_f32_e32 v121, v100, v121
	v_add_f32_e32 v122, v100, v122
	v_add_f32_e32 v123, v100, v123
	v_cvt_pk_f16_f32 v120, v120, v121
	v_cvt_pk_f16_f32 v121, v122, v123
	v_cvt_pk_f16_f32 v122, v116, v117
	v_cvt_pk_f16_f32 v123, v118, v119
	v_pk_max_f16 v120, v120, 0
	v_pk_max_f16 v121, v121, 0
	v_pk_max_f16 v122, v122, 0
	v_pk_max_f16 v123, v123, 0
	s_nop 1
	v_mfma_f32_16x16x32_f16 v[0:3], v[120:123], v[66:69], v[0:3]
	s_andn2_b64 exec, exec, s[12:13]
	s_cbranch_execz .LBB5_43

	.amdhsa_kernel _Z5k_gcnILi2EEvPKvPK15HIP_vector_typeIiLj2EEPfPKiS8_PKfPKDF16_SA_SA_SA_SA_S6_PDF16_S6_SD_SC_SA_
		.amdhsa_group_segment_fixed_size 23808
		.amdhsa_private_segment_fixed_size 0
		.amdhsa_kernarg_size 392
		.amdhsa_user_sgpr_count 2
		.amdhsa_user_sgpr_dispatch_ptr 0
		.amdhsa_user_sgpr_queue_ptr 0
		.amdhsa_user_sgpr_kernarg_segment_ptr 1
		.amdhsa_user_sgpr_dispatch_id 0
		.amdhsa_user_sgpr_kernarg_preload_length 0
		.amdhsa_user_sgpr_kernarg_preload_offset 0
		.amdhsa_user_sgpr_private_segment_size 0
		.amdhsa_uses_dynamic_stack 0
		.amdhsa_enable_private_segment 0
		.amdhsa_system_sgpr_workgroup_id_x 1
		.amdhsa_system_sgpr_workgroup_id_y 0
		.amdhsa_system_sgpr_workgroup_id_z 0
		.amdhsa_system_sgpr_workgroup_info 0
		.amdhsa_system_vgpr_workitem_id 2
		.amdhsa_next_free_vgpr 124
		.amdhsa_next_free_sgpr 91
		.amdhsa_accum_offset 124
		.amdhsa_reserve_vcc 1
		.amdhsa_float_round_mode_32 0
		.amdhsa_float_round_mode_16_64 0
		.amdhsa_float_denorm_mode_32 3
		.amdhsa_float_denorm_mode_16_64 3
		.amdhsa_dx10_clamp 1
		.amdhsa_ieee_mode 1
		.amdhsa_fp16_overflow 0
		.amdhsa_tg_split 0
		.amdhsa_exception_fp_ieee_invalid_op 0
		.amdhsa_exception_fp_denorm_src 0
		.amdhsa_exception_fp_ieee_div_zero 0
		.amdhsa_exception_fp_ieee_overflow 0
		.amdhsa_exception_fp_ieee_underflow 0
		.amdhsa_exception_fp_ieee_inexact 0
		.amdhsa_exception_int_div_zero 0
	.end_amdhsa_kernel

amdhsa.kernels:
  - .agpr_count:     0
    .args:
      - .actual_access:  read_only
        .address_space:  global
        .offset:         0
        .size:           8
        .value_kind:     global_buffer
      - .actual_access:  read_only
        .address_space:  global
        .offset:         8
        .size:           8
        .value_kind:     global_buffer
      - .actual_access:  read_only
        .address_space:  global
        .offset:         16
        .size:           8
        .value_kind:     global_buffer
      - .actual_access:  read_only
        .address_space:  global
        .offset:         24
        .size:           8
        .value_kind:     global_buffer
      - .actual_access:  write_only
        .address_space:  global
        .offset:         32
        .size:           8
        .value_kind:     global_buffer
      - .actual_access:  write_only
        .address_space:  global
        .offset:         40
        .size:           8
        .value_kind:     global_buffer
    .group_segment_fixed_size: 56512
    .kernarg_segment_align: 8
    .kernarg_segment_size: 48
    .language:       OpenCL C
    .language_version:
      - 2
      - 0
    .max_flat_workgroup_size: 1024
    .name:           _Z10k_bscatterPKiS0_PKfS0_PiP15HIP_vector_typeIiLj2EE
    .private_segment_fixed_size: 0
    .sgpr_count:     42
    .sgpr_spill_count: 0
    .symbol:         _Z10k_bscatterPKiS0_PKfS0_PiP15HIP_vector_typeIiLj2EE.kd
    .uniform_work_group_size: 1
    .uses_dynamic_stack: false
    .vgpr_count:     89
    .vgpr_spill_count: 0
    .wavefront_size: 64
  - .agpr_count:     0
    .args:
      - .actual_access:  read_only
        .address_space:  global
        .offset:         0
        .size:           8
        .value_kind:     global_buffer
      - .actual_access:  read_only
        .address_space:  global
        .offset:         8
        .size:           8
        .value_kind:     global_buffer
      - .actual_access:  write_only
        .address_space:  global
        .offset:         16
        .size:           8
        .value_kind:     global_buffer
      - .actual_access:  write_only
        .address_space:  global
        .offset:         24
        .size:           8
        .value_kind:     global_buffer
      - .actual_access:  write_only
        .address_space:  global
        .offset:         32
        .size:           8
        .value_kind:     global_buffer
      - .actual_access:  write_only
        .address_space:  global
        .offset:         40
        .size:           8
        .value_kind:     global_buffer
      - .actual_access:  read_only
        .address_space:  global
        .offset:         48
        .size:           8
        .value_kind:     global_buffer
      - .actual_access:  write_only
        .address_space:  global
        .offset:         56
        .size:           8
        .value_kind:     global_buffer
    .group_segment_fixed_size: 12352
    .kernarg_segment_align: 8
    .kernarg_segment_size: 64
    .language:       OpenCL C
    .language_version:
      - 2
      - 0
    .max_flat_workgroup_size: 1024
    .name:           _Z8k_bfinalPK15HIP_vector_typeIiLj2EEPKiPS0_PiS6_PfPKfPDF16_
    .private_segment_fixed_size: 0
    .sgpr_count:     38
    .sgpr_spill_count: 0
    .symbol:         _Z8k_bfinalPK15HIP_vector_typeIiLj2EEPKiPS0_PiS6_PfPKfPDF16_.kd
    .uniform_work_group_size: 1
    .uses_dynamic_stack: false
    .vgpr_count:     72
    .vgpr_spill_count: 0
    .wavefront_size: 64
  - .agpr_count:     0
    .args:
      - .actual_access:  read_only
        .address_space:  global
        .offset:         0
        .size:           8
        .value_kind:     global_buffer
      - .actual_access:  write_only
        .address_space:  global
        .offset:         8
        .size:           8
        .value_kind:     global_buffer
      - .actual_access:  write_only
        .address_space:  global
        .offset:         16
        .size:           8
        .value_kind:     global_buffer
      - .actual_access:  read_only
        .address_space:  global
        .offset:         24
        .size:           8
        .value_kind:     global_buffer
      - .actual_access:  read_only
        .address_space:  global
        .offset:         32
        .size:           8
        .value_kind:     global_buffer
      - .actual_access:  write_only
        .address_space:  global
        .offset:         40
        .size:           8
        .value_kind:     global_buffer
      - .actual_access:  read_only
        .address_space:  global
        .offset:         48
        .size:           8
        .value_kind:     global_buffer
      - .actual_access:  read_only
        .address_space:  global
        .offset:         56
        .size:           8
        .value_kind:     global_buffer
      - .actual_access:  read_only
        .address_space:  global
        .offset:         64
        .size:           8
        .value_kind:     global_buffer
      - .actual_access:  read_only
        .address_space:  global
        .offset:         72
        .size:           8
        .value_kind:     global_buffer
      - .actual_access:  read_only
        .address_space:  global
        .offset:         80
        .size:           8
        .value_kind:     global_buffer
      - .actual_access:  read_only
        .address_space:  global
        .offset:         88
        .size:           8
        .value_kind:     global_buffer
      - .actual_access:  write_only
        .address_space:  global
        .offset:         96
        .size:           8
        .value_kind:     global_buffer
      - .actual_access:  write_only
        .address_space:  global
        .offset:         104
        .size:           8
        .value_kind:     global_buffer
      - .actual_access:  write_only
        .address_space:  global
        .offset:         112
        .size:           8
        .value_kind:     global_buffer
      - .actual_access:  write_only
        .address_space:  global
        .offset:         120
        .size:           8
        .value_kind:     global_buffer
      - .actual_access:  write_only
        .address_space:  global
        .offset:         128
        .size:           8
        .value_kind:     global_buffer
    .group_segment_fixed_size: 628
    .kernarg_segment_align: 8
    .kernarg_segment_size: 136
    .language:       OpenCL C
    .language_version:
      - 2
      - 0
    .max_flat_workgroup_size: 1024
    .name:           _Z7k_bhistPKiPiPfPKfS4_PDF16_S4_S4_S4_S4_S4_S4_S5_S5_S5_S5_S2_
    .private_segment_fixed_size: 0
    .sgpr_count:     25
    .sgpr_spill_count: 0
    .symbol:         _Z7k_bhistPKiPiPfPKfS4_PDF16_S4_S4_S4_S4_S4_S4_S5_S5_S5_S5_S2_.kd
    .uniform_work_group_size: 1
    .uses_dynamic_stack: false
    .vgpr_count:     32
    .vgpr_spill_count: 0
    .wavefront_size: 64
  - .agpr_count:     0
    .args:
      - .actual_access:  read_only
        .address_space:  global
        .offset:         0
        .size:           8
        .value_kind:     global_buffer
      - .actual_access:  read_only
        .address_space:  global
        .offset:         8
        .size:           8
        .value_kind:     global_buffer
      - .actual_access:  read_only
        .address_space:  global
        .offset:         16
        .size:           8
        .value_kind:     global_buffer
      - .actual_access:  read_only
        .address_space:  global
        .offset:         24
        .size:           8
        .value_kind:     global_buffer
      - .actual_access:  read_only
        .address_space:  global
        .offset:         32
        .size:           8
        .value_kind:     global_buffer
      - .actual_access:  read_only
        .address_space:  global
        .offset:         40
        .size:           8
        .value_kind:     global_buffer
      - .actual_access:  read_only
        .address_space:  global
        .offset:         48
        .size:           8
        .value_kind:     global_buffer
      - .actual_access:  read_only
        .address_space:  global
        .offset:         56
        .size:           8
        .value_kind:     global_buffer
      - .actual_access:  read_only
        .address_space:  global
        .offset:         64
        .size:           8
        .value_kind:     global_buffer
      - .actual_access:  write_only
        .address_space:  global
        .offset:         72
        .size:           8
        .value_kind:     global_buffer
      - .actual_access:  write_only
        .address_space:  global
        .offset:         80
        .size:           8
        .value_kind:     global_buffer
      - .offset:         88
        .size:           4
        .value_kind:     hidden_block_count_x
      - .offset:         92
        .size:           4
        .value_kind:     hidden_block_count_y
      - .offset:         96
        .size:           4
        .value_kind:     hidden_block_count_z
      - .offset:         100
        .size:           2
        .value_kind:     hidden_group_size_x
      - .offset:         102
        .size:           2
        .value_kind:     hidden_group_size_y
      - .offset:         104
        .size:           2
        .value_kind:     hidden_group_size_z
      - .offset:         106
        .size:           2
        .value_kind:     hidden_remainder_x
      - .offset:         108
        .size:           2
        .value_kind:     hidden_remainder_y
      - .offset:         110
        .size:           2
        .value_kind:     hidden_remainder_z
      - .offset:         128
        .size:           8
        .value_kind:     hidden_global_offset_x
      - .offset:         136
        .size:           8
        .value_kind:     hidden_global_offset_y
      - .offset:         144
        .size:           8
        .value_kind:     hidden_global_offset_z
      - .offset:         152
        .size:           2
        .value_kind:     hidden_grid_dims
    .group_segment_fixed_size: 2048
    .kernarg_segment_align: 8
    .kernarg_segment_size: 344
    .language:       OpenCL C
    .language_version:
      - 2
      - 0
    .max_flat_workgroup_size: 256
    .name:           _Z7k_fold2PKfS0_S0_S0_S0_S0_S0_S0_S0_PDF16_Pf
    .private_segment_fixed_size: 0
    .sgpr_count:     36
    .sgpr_spill_count: 0
    .symbol:         _Z7k_fold2PKfS0_S0_S0_S0_S0_S0_S0_S0_PDF16_Pf.kd
    .uniform_work_group_size: 1
    .uses_dynamic_stack: false
    .vgpr_count:     61
    .vgpr_spill_count: 0
    .wavefront_size: 64
  - .agpr_count:     0
    .args:
      - .actual_access:  read_only
        .address_space:  global
        .offset:         0
        .size:           8
        .value_kind:     global_buffer
      - .actual_access:  read_only
        .address_space:  global
        .offset:         8
        .size:           8
        .value_kind:     global_buffer
      - .actual_access:  write_only
        .address_space:  global
        .offset:         16
        .size:           8
        .value_kind:     global_buffer
      - .actual_access:  read_only
        .address_space:  global
        .offset:         24
        .size:           8
        .value_kind:     global_buffer
      - .actual_access:  read_only
        .address_space:  global
        .offset:         32
        .size:           8
        .value_kind:     global_buffer
      - .actual_access:  read_only
        .address_space:  global
        .offset:         40
        .size:           8
        .value_kind:     global_buffer
      - .actual_access:  read_only
        .address_space:  global
        .offset:         48
        .size:           8
        .value_kind:     global_buffer
      - .actual_access:  read_only
        .address_space:  global
        .offset:         56
        .size:           8
        .value_kind:     global_buffer
      - .actual_access:  read_only
        .address_space:  global
        .offset:         64
        .size:           8
        .value_kind:     global_buffer
      - .actual_access:  read_only
        .address_space:  global
        .offset:         72
        .size:           8
        .value_kind:     global_buffer
      - .actual_access:  read_only
        .address_space:  global
        .offset:         80
        .size:           8
        .value_kind:     global_buffer
      - .actual_access:  write_only
        .address_space:  global
        .offset:         88
        .size:           8
        .value_kind:     global_buffer
      - .actual_access:  write_only
        .address_space:  global
        .offset:         96
        .size:           8
        .value_kind:     global_buffer
      - .address_space:  global
        .offset:         104
        .size:           8
        .value_kind:     global_buffer
      - .actual_access:  write_only
        .address_space:  global
        .offset:         112
        .size:           8
        .value_kind:     global_buffer
      - .actual_access:  read_only
        .address_space:  global
        .offset:         120
        .size:           8
        .value_kind:     global_buffer
      - .actual_access:  read_only
        .address_space:  global
        .offset:         128
        .size:           8
        .value_kind:     global_buffer
    .group_segment_fixed_size: 22272
    .kernarg_segment_align: 8
    .kernarg_segment_size: 136
    .language:       OpenCL C
    .language_version:
      - 2
      - 0
    .max_flat_workgroup_size: 256
    .name:           _Z5k_gcnILi1EEvPKvPK15HIP_vector_typeIiLj2EEPfPKiS8_PKfPKDF16_SA_SA_SA_SA_S6_PDF16_S6_SD_SC_SA_
    .private_segment_fixed_size: 0
    .sgpr_count:     35
    .sgpr_spill_count: 0
    .symbol:         _Z5k_gcnILi1EEvPKvPK15HIP_vector_typeIiLj2EEPfPKiS8_PKfPKDF16_SA_SA_SA_SA_S6_PDF16_S6_SD_SC_SA_.kd
    .uniform_work_group_size: 1
    .uses_dynamic_stack: false
    .vgpr_count:     58
    .vgpr_spill_count: 0
    .wavefront_size: 64
  - .agpr_count:     0
    .args:
      - .actual_access:  read_only
        .address_space:  global
        .offset:         0
        .size:           8
        .value_kind:     global_buffer
      - .actual_access:  read_only
        .address_space:  global
        .offset:         8
        .size:           8
        .value_kind:     global_buffer
      - .actual_access:  read_only
        .address_space:  global
        .offset:         16
        .size:           8
        .value_kind:     global_buffer
      - .actual_access:  read_only
        .address_space:  global
        .offset:         24
        .size:           8
        .value_kind:     global_buffer
      - .actual_access:  read_only
        .address_space:  global
        .offset:         32
        .size:           8
        .value_kind:     global_buffer
      - .actual_access:  read_only
        .address_space:  global
        .offset:         40
        .size:           8
        .value_kind:     global_buffer
      - .actual_access:  read_only
        .address_space:  global
        .offset:         48
        .size:           8
        .value_kind:     global_buffer
      - .actual_access:  read_only
        .address_space:  global
        .offset:         56
        .size:           8
        .value_kind:     global_buffer
      - .actual_access:  read_only
        .address_space:  global
        .offset:         64
        .size:           8
        .value_kind:     global_buffer
      - .actual_access:  read_only
        .address_space:  global
        .offset:         72
        .size:           8
        .value_kind:     global_buffer
      - .actual_access:  read_only
        .address_space:  global
        .offset:         80
        .size:           8
        .value_kind:     global_buffer
      - .actual_access:  read_only
        .address_space:  global
        .offset:         88
        .size:           8
        .value_kind:     global_buffer
      - .actual_access:  write_only
        .address_space:  global
        .offset:         96
        .size:           8
        .value_kind:     global_buffer
      - .address_space:  global
        .offset:         104
        .size:           8
        .value_kind:     global_buffer
      - .actual_access:  read_only
        .address_space:  global
        .offset:         112
        .size:           8
        .value_kind:     global_buffer
      - .actual_access:  read_only
        .address_space:  global
        .offset:         120
        .size:           8
        .value_kind:     global_buffer
      - .actual_access:  read_only
        .address_space:  global
        .offset:         128
        .size:           8
        .value_kind:     global_buffer
      - .offset:         136
        .size:           4
        .value_kind:     hidden_block_count_x
      - .offset:         140
        .size:           4
        .value_kind:     hidden_block_count_y
      - .offset:         144
        .size:           4
        .value_kind:     hidden_block_count_z
      - .offset:         148
        .size:           2
        .value_kind:     hidden_group_size_x
      - .offset:         150
        .size:           2
        .value_kind:     hidden_group_size_y
      - .offset:         152
        .size:           2
        .value_kind:     hidden_group_size_z
      - .offset:         154
        .size:           2
        .value_kind:     hidden_remainder_x
      - .offset:         156
        .size:           2
        .value_kind:     hidden_remainder_y
      - .offset:         158
        .size:           2
        .value_kind:     hidden_remainder_z
      - .offset:         176
        .size:           8
        .value_kind:     hidden_global_offset_x
      - .offset:         184
        .size:           8
        .value_kind:     hidden_global_offset_y
      - .offset:         192
        .size:           8
        .value_kind:     hidden_global_offset_z
      - .offset:         200
        .size:           2
        .value_kind:     hidden_grid_dims
    .group_segment_fixed_size: 23808
    .kernarg_segment_align: 8
    .kernarg_segment_size: 392
    .language:       OpenCL C
    .language_version:
      - 2
      - 0
    .max_flat_workgroup_size: 256
    .name:           _Z5k_gcnILi2EEvPKvPK15HIP_vector_typeIiLj2EEPfPKiS8_PKfPKDF16_SA_SA_SA_SA_S6_PDF16_S6_SD_SC_SA_
    .private_segment_fixed_size: 0
    .sgpr_count:     36
    .sgpr_spill_count: 0
    .symbol:         _Z5k_gcnILi2EEvPKvPK15HIP_vector_typeIiLj2EEPfPKiS8_PKfPKDF16_SA_SA_SA_SA_S6_PDF16_S6_SD_SC_SA_.kd
    .uniform_work_group_size: 1
    .uses_dynamic_stack: false
    .vgpr_count:     124
    .vgpr_spill_count: 0
    .wavefront_size: 64
  - .agpr_count:     0
    .args:
      - .actual_access:  read_only
        .address_space:  global
        .offset:         0
        .size:           8
        .value_kind:     global_buffer
      - .actual_access:  read_only
        .address_space:  global
        .offset:         8
        .size:           8
        .value_kind:     global_buffer
      - .actual_access:  read_only
        .address_space:  global
        .offset:         16
        .size:           8
        .value_kind:     global_buffer
      - .actual_access:  read_only
        .address_space:  global
        .offset:         24
        .size:           8
        .value_kind:     global_buffer
      - .actual_access:  write_only
        .address_space:  global
        .offset:         32
        .size:           8
        .value_kind:     global_buffer
      - .actual_access:  read_only
        .address_space:  global
        .offset:         40
        .size:           8
        .value_kind:     global_buffer
      - .actual_access:  read_only
        .address_space:  global
        .offset:         48
        .size:           8
        .value_kind:     global_buffer
      - .actual_access:  read_only
        .address_space:  global
        .offset:         56
        .size:           8
        .value_kind:     global_buffer
      - .actual_access:  read_only
        .address_space:  global
        .offset:         64
        .size:           8
        .value_kind:     global_buffer
      - .actual_access:  read_only
        .address_space:  global
        .offset:         72
        .size:           8
        .value_kind:     global_buffer
      - .actual_access:  read_only
        .address_space:  global
        .offset:         80
        .size:           8
        .value_kind:     global_buffer
      - .actual_access:  read_only
        .address_space:  global
        .offset:         88
        .size:           8
        .value_kind:     global_buffer
      - .actual_access:  write_only
        .address_space:  global
        .offset:         96
        .size:           8
        .value_kind:     global_buffer
    .group_segment_fixed_size: 9216
    .kernarg_segment_align: 8
    .kernarg_segment_size: 104
    .language:       OpenCL C
    .language_version:
      - 2
      - 0
    .max_flat_workgroup_size: 512
    .name:           _Z6k_lstmILi256ELi10ELb1ELb0EEvPKDF16_S1_S1_PKfPDF16_S1_S1_S1_S3_S3_S3_PfS5_
    .private_segment_fixed_size: 0
    .sgpr_count:     37
    .sgpr_spill_count: 0
    .symbol:         _Z6k_lstmILi256ELi10ELb1ELb0EEvPKDF16_S1_S1_PKfPDF16_S1_S1_S1_S3_S3_S3_PfS5_.kd
    .uniform_work_group_size: 1
    .uses_dynamic_stack: false
    .vgpr_count:     256
    .vgpr_spill_count: 0
    .wavefront_size: 64
  - .agpr_count:     0
    .args:
      - .actual_access:  read_only
        .address_space:  global
        .offset:         0
        .size:           8
        .value_kind:     global_buffer
      - .actual_access:  read_only
        .address_space:  global
        .offset:         8
        .size:           8
        .value_kind:     global_buffer
      - .actual_access:  read_only
        .address_space:  global
        .offset:         16
        .size:           8
        .value_kind:     global_buffer
      - .actual_access:  read_only
        .address_space:  global
        .offset:         24
        .size:           8
        .value_kind:     global_buffer
      - .actual_access:  read_only
        .address_space:  global
        .offset:         32
        .size:           8
        .value_kind:     global_buffer
      - .actual_access:  read_only
        .address_space:  global
        .offset:         40
        .size:           8
        .value_kind:     global_buffer
      - .actual_access:  read_only
        .address_space:  global
        .offset:         48
        .size:           8
        .value_kind:     global_buffer
      - .actual_access:  read_only
        .address_space:  global
        .offset:         56
        .size:           8
        .value_kind:     global_buffer
      - .actual_access:  read_only
        .address_space:  global
        .offset:         64
        .size:           8
        .value_kind:     global_buffer
      - .actual_access:  read_only
        .address_space:  global
        .offset:         72
        .size:           8
        .value_kind:     global_buffer
      - .actual_access:  read_only
        .address_space:  global
        .offset:         80
        .size:           8
        .value_kind:     global_buffer
      - .actual_access:  write_only
        .address_space:  global
        .offset:         88
        .size:           8
        .value_kind:     global_buffer
      - .actual_access:  read_only
        .address_space:  global
        .offset:         96
        .size:           8
        .value_kind:     global_buffer
    .group_segment_fixed_size: 0
    .kernarg_segment_align: 8
    .kernarg_segment_size: 104
    .language:       OpenCL C
    .language_version:
      - 2
      - 0
    .max_flat_workgroup_size: 512
    .name:           _Z6k_lstmILi128ELi8ELb0ELb1EEvPKDF16_S1_S1_PKfPDF16_S1_S1_S1_S3_S3_S3_PfS5_
    .private_segment_fixed_size: 0
    .sgpr_count:     42
    .sgpr_spill_count: 0
    .symbol:         _Z6k_lstmILi128ELi8ELb0ELb1EEvPKDF16_S1_S1_PKfPDF16_S1_S1_S1_S3_S3_S3_PfS5_.kd
    .uniform_work_group_size: 1
    .uses_dynamic_stack: false
    .vgpr_count:     224
    .vgpr_spill_count: 0
    .wavefront_size: 64
